# ALiBi A-operand build in the attention sub-tiles: lane mask dropped (the B operand is already zero on those lanes) and redundant byte-convert mask removed: 5 -> 3 VALU
# speedup vs baseline: 1.0083x; 1.0081x over previous
.LBB0_447:
	s_add_i32 s2, s26, s23
	s_and_b32 s3, s30, 0x18000
	s_add_i32 s3, s3, 0
	s_add_i32 s33, s3, s27
	v_add_u32_e32 v2, s33, v162
	v_add_u32_e32 v4, s33, v164
	v_add_u32_e32 v5, s33, v165
	v_add_u32_e32 v70, s33, v166
	s_ashr_i32 s33, s31, 2
	v_cvt_f32_i32_e32 v170, s33
	v_add_u32_e32 v106, s3, v160
	s_add_i32 s3, s2, 0x7e0
	v_add_u32_e32 v169, 0x4000, v106
	s_cmp_gt_i32 s3, s28
	v_add_u32_e32 v174, v2, v145
	v_add_u32_e32 v173, v4, v145
	v_add_u32_e32 v172, v5, v145
	v_add_u32_e32 v171, v70, v145
	s_barrier
	s_cbranch_scc1 .LBB0_455
	ds_read_b128 v[70:73], v174 offset:4096
	ds_read_b128 v[188:191], v173 offset:4096
	ds_read_b128 v[192:195], v172 offset:4096
	ds_read_b128 v[202:205], v171 offset:4096
	s_and_b32 s3, s3, 0xe0
	v_or_b32_e32 v2, s3, v159
	v_cvt_f32_ubyte0_e32 v2, v2
	v_or_b32_sdwa v2, v2, v170 dst_sel:DWORD dst_unused:UNUSED_PAD src0_sel:DWORD src1_sel:WORD_1
	v_mov_b32_e32 v4, v3
	s_waitcnt lgkmcnt(3)
	s_setprio 1
	v_mfma_f32_32x32x16_bf16 v[70:85], v[70:73], v[86:89], 0
	v_mov_b32_e32 v5, v3
	s_add_i32 s3, s2, 0x7ff
	s_cmp_ge_i32 s19, s3
	s_cselect_b64 s[40:41], -1, 0
	s_add_i32 s3, s29, 0xffffffa0
	s_cmp_lt_i32 s3, 0x3fffffe1
	v_add_u32_e32 v175, v169, v150
	s_waitcnt lgkmcnt(2)
	v_mfma_f32_32x32x16_bf16 v[70:85], v[188:191], v[90:93], v[70:85]
	s_cselect_b64 s[42:43], -1, 0
	s_and_b64 s[40:41], s[40:41], s[42:43]
	s_and_b64 vcc, exec, s[40:41]
	s_waitcnt lgkmcnt(1)
	v_mfma_f32_32x32x16_bf16 v[70:85], v[192:195], v[94:97], v[70:85]
	s_waitcnt lgkmcnt(0)
	v_mfma_f32_32x32x16_bf16 v[70:85], v[202:205], v[98:101], v[70:85]
	v_mfma_f32_32x32x16_bf16 v[70:85], v[2:5], v[102:105], v[70:85]
	v_add3_u32 v2, v106, v142, s68
	v_add_u32_e32 v4, v169, v146
	v_add_u32_e32 v5, v169, v148
	ds_read_b64_tr_b16 v[134:135], v2
	ds_read_b64_tr_b16 v[136:137], v2 offset:2048
	ds_read_b64_tr_b16 v[130:131], v4
	ds_read_b64_tr_b16 v[132:133], v4 offset:2048
	ds_read_b64_tr_b16 v[126:127], v5
	ds_read_b64_tr_b16 v[128:129], v5 offset:2048
	ds_read_b64_tr_b16 v[122:123], v175
	ds_read_b64_tr_b16 v[124:125], v175 offset:2048
	ds_read_b64_tr_b16 v[118:119], v2 offset:4096
	ds_read_b64_tr_b16 v[120:121], v2 offset:6144
	ds_read_b64_tr_b16 v[114:115], v4 offset:4096
	ds_read_b64_tr_b16 v[116:117], v4 offset:6144
	ds_read_b64_tr_b16 v[110:111], v5 offset:4096
	ds_read_b64_tr_b16 v[112:113], v5 offset:6144
	ds_read_b64_tr_b16 v[106:107], v175 offset:4096
	ds_read_b64_tr_b16 v[108:109], v175 offset:6144
	s_cbranch_vccnz .LBB0_452
	v_add_u32_e32 v2, s29, v161
	v_add_u32_e32 v4, 0xffffffa0, v2
	v_cmp_gt_u32_e32 vcc, 2.0, v4
	v_add_u32_e32 v4, s23, v163
	v_add_u32_e32 v4, 0x60, v4
	s_nop 2
	v_cndmask_b32_e32 v70, v197, v70, vcc
	v_cmp_lt_u32_e32 vcc, s75, v4
	v_add_u32_e32 v4, 0xffffff9e, v2
	s_nop 0
	v_cndmask_b32_e32 v71, v197, v71, vcc
	v_cmp_gt_u32_e32 vcc, 2.0, v4
	v_add_u32_e32 v4, 0xffffff9d, v2
	s_nop 0
	v_cndmask_b32_e32 v72, v197, v72, vcc
	v_cmp_gt_u32_e32 vcc, 2.0, v4
	v_add_u32_e32 v4, 0xffffff98, v2
	s_nop 0
	v_cndmask_b32_e32 v73, v197, v73, vcc
	v_cmp_gt_u32_e32 vcc, 2.0, v4
	v_add_u32_e32 v4, 0xffffff97, v2
	s_nop 0
	v_cndmask_b32_e32 v74, v197, v74, vcc
	v_cmp_gt_u32_e32 vcc, 2.0, v4
	v_add_u32_e32 v4, 0xffffff96, v2
	s_nop 0
	v_cndmask_b32_e32 v75, v197, v75, vcc
	v_cmp_gt_u32_e32 vcc, 2.0, v4
	v_add_u32_e32 v4, 0xffffff95, v2
	s_nop 0
	v_cndmask_b32_e32 v76, v197, v76, vcc
	v_cmp_gt_u32_e32 vcc, 2.0, v4
	v_add_u32_e32 v4, 0xffffff90, v2
	s_nop 0
	v_cndmask_b32_e32 v77, v197, v77, vcc
	v_cmp_gt_u32_e32 vcc, 2.0, v4
	v_add_u32_e32 v4, 0xffffff8f, v2
	s_nop 0
	v_cndmask_b32_e32 v78, v197, v78, vcc
	v_cmp_gt_u32_e32 vcc, 2.0, v4
	v_add_u32_e32 v4, 0xffffff8e, v2
	s_nop 0
	v_cndmask_b32_e32 v79, v197, v79, vcc
	v_cmp_gt_u32_e32 vcc, 2.0, v4
	v_add_u32_e32 v4, 0xffffff8d, v2
	s_nop 0
	v_cndmask_b32_e32 v80, v197, v80, vcc
	v_cmp_gt_u32_e32 vcc, 2.0, v4
	v_add_u32_e32 v4, 0xffffff88, v2
	s_nop 0
	v_cndmask_b32_e32 v81, v197, v81, vcc
	v_cmp_gt_u32_e32 vcc, 2.0, v4
	v_add_u32_e32 v4, 0xffffff87, v2
	s_nop 0
	v_cndmask_b32_e32 v82, v197, v82, vcc
	v_cmp_gt_u32_e32 vcc, 2.0, v4
	v_add_u32_e32 v4, 0xffffff86, v2
	v_add_u32_e32 v2, 0xffffff85, v2
	v_cndmask_b32_e32 v83, v197, v83, vcc
	v_cmp_gt_u32_e32 vcc, 2.0, v4
	s_nop 1
	v_cndmask_b32_e32 v84, v197, v84, vcc
	v_cmp_gt_u32_e32 vcc, 2.0, v2
	s_nop 1
	v_cndmask_b32_e32 v85, v197, v85, vcc

.Lring_issue_skip_2:
	s_add_i32 s3, s2, 0x7c0
	s_cmp_gt_i32 s3, s28
	s_cbranch_scc1 .LBB0_461
	ds_read_b128 v[70:73], v174
	ds_read_b128 v[188:191], v173
	ds_read_b128 v[192:195], v172
	ds_read_b128 v[202:205], v171
	s_and_b32 s3, s3, 0xc0
	v_or_b32_e32 v2, s3, v159
	v_cvt_f32_ubyte0_e32 v2, v2
	v_or_b32_sdwa v2, v2, v170 dst_sel:DWORD dst_unused:UNUSED_PAD src0_sel:DWORD src1_sel:WORD_1
	v_mov_b32_e32 v4, v3
	s_waitcnt lgkmcnt(3)
	s_setprio 1
	v_mfma_f32_32x32x16_bf16 v[70:85], v[70:73], v[86:89], 0
	v_mov_b32_e32 v5, v3
	s_addk_i32 s2, 0x7df
	s_cmp_ge_i32 s19, s2
	s_cselect_b64 s[2:3], -1, 0
	s_sub_i32 s33, s29, 64
	s_cmp_lt_i32 s33, 0x3fffffe1
	s_cselect_b64 s[40:41], -1, 0
	s_waitcnt lgkmcnt(2)
	v_mfma_f32_32x32x16_bf16 v[70:85], v[188:191], v[90:93], v[70:85]
	s_and_b64 s[2:3], s[2:3], s[40:41]
	s_and_b64 vcc, exec, s[2:3]
	s_waitcnt lgkmcnt(1)
	v_mfma_f32_32x32x16_bf16 v[70:85], v[192:195], v[94:97], v[70:85]
	s_waitcnt lgkmcnt(0)
	v_mfma_f32_32x32x16_bf16 v[70:85], v[202:205], v[98:101], v[70:85]
	v_mfma_f32_32x32x16_bf16 v[70:85], v[2:5], v[102:105], v[70:85]
	v_add_u32_e32 v2, v169, v142
	v_add_u32_e32 v4, v169, v152
	v_add_u32_e32 v5, v169, v154
	v_add_u32_e32 v169, v169, v156
	ds_read_b64_tr_b16 v[134:135], v2
	ds_read_b64_tr_b16 v[136:137], v2 offset:2048
	ds_read_b64_tr_b16 v[130:131], v4
	ds_read_b64_tr_b16 v[132:133], v4 offset:2048
	ds_read_b64_tr_b16 v[126:127], v5
	ds_read_b64_tr_b16 v[128:129], v5 offset:2048
	ds_read_b64_tr_b16 v[122:123], v169
	ds_read_b64_tr_b16 v[124:125], v169 offset:2048
	ds_read_b64_tr_b16 v[118:119], v2 offset:4096
	ds_read_b64_tr_b16 v[120:121], v2 offset:6144
	ds_read_b64_tr_b16 v[114:115], v4 offset:4096
	ds_read_b64_tr_b16 v[116:117], v4 offset:6144
	ds_read_b64_tr_b16 v[110:111], v5 offset:4096
	ds_read_b64_tr_b16 v[112:113], v5 offset:6144
	ds_read_b64_tr_b16 v[106:107], v169 offset:4096
	ds_read_b64_tr_b16 v[108:109], v169 offset:6144
	s_cbranch_vccnz .LBB0_458
	v_add_u32_e32 v2, s29, v161
	v_subrev_u32_e32 v4, 64, v2
	v_cmp_gt_u32_e32 vcc, 2.0, v4
	v_add3_u32 v4, v163, s23, 64
	s_nop 2
	v_cndmask_b32_e32 v70, v197, v70, vcc
	v_cmp_lt_u32_e32 vcc, s75, v4
	v_add_u32_e32 v4, 0xffffffbe, v2
	s_nop 0
	v_cndmask_b32_e32 v71, v197, v71, vcc
	v_cmp_gt_u32_e32 vcc, 2.0, v4
	v_add_u32_e32 v4, 0xffffffbd, v2
	s_nop 0
	v_cndmask_b32_e32 v72, v197, v72, vcc
	v_cmp_gt_u32_e32 vcc, 2.0, v4
	v_add_u32_e32 v4, 0xffffffb8, v2
	s_nop 0
	v_cndmask_b32_e32 v73, v197, v73, vcc
	v_cmp_gt_u32_e32 vcc, 2.0, v4
	v_add_u32_e32 v4, 0xffffffb7, v2
	s_nop 0
	v_cndmask_b32_e32 v74, v197, v74, vcc
	v_cmp_gt_u32_e32 vcc, 2.0, v4
	v_add_u32_e32 v4, 0xffffffb6, v2
	s_nop 0
	v_cndmask_b32_e32 v75, v197, v75, vcc
	v_cmp_gt_u32_e32 vcc, 2.0, v4
	v_add_u32_e32 v4, 0xffffffb5, v2
	s_nop 0
	v_cndmask_b32_e32 v76, v197, v76, vcc
	v_cmp_gt_u32_e32 vcc, 2.0, v4
	v_add_u32_e32 v4, 0xffffffb0, v2
	s_nop 0
	v_cndmask_b32_e32 v77, v197, v77, vcc
	v_cmp_gt_u32_e32 vcc, 2.0, v4
	v_add_u32_e32 v4, 0xffffffaf, v2
	s_nop 0
	v_cndmask_b32_e32 v78, v197, v78, vcc
	v_cmp_gt_u32_e32 vcc, 2.0, v4
	v_add_u32_e32 v4, 0xffffffae, v2
	s_nop 0
	v_cndmask_b32_e32 v79, v197, v79, vcc
	v_cmp_gt_u32_e32 vcc, 2.0, v4
	v_add_u32_e32 v4, 0xffffffad, v2
	s_nop 0
	v_cndmask_b32_e32 v80, v197, v80, vcc
	v_cmp_gt_u32_e32 vcc, 2.0, v4
	v_add_u32_e32 v4, 0xffffffa8, v2
	s_nop 0
	v_cndmask_b32_e32 v81, v197, v81, vcc
	v_cmp_gt_u32_e32 vcc, 2.0, v4
	v_add_u32_e32 v4, 0xffffffa7, v2
	s_nop 0
	v_cndmask_b32_e32 v82, v197, v82, vcc
	v_cmp_gt_u32_e32 vcc, 2.0, v4
	v_add_u32_e32 v4, 0xffffffa6, v2
	v_add_u32_e32 v2, 0xffffffa5, v2
	v_cndmask_b32_e32 v83, v197, v83, vcc
	v_cmp_gt_u32_e32 vcc, 2.0, v4
	s_nop 1
	v_cndmask_b32_e32 v84, v197, v84, vcc
	v_cmp_gt_u32_e32 vcc, 2.0, v2
	s_nop 1
	v_cndmask_b32_e32 v85, v197, v85, vcc

.Lw_win_4_done:
.LBB0_519:
	s_cmp_eq_u32 s32, 0
	s_cselect_b32 s84, 0, 1
	s_sub_u32 s32, s32, s84
	s_add_i32 s2, s29, s22
	s_add_i32 s3, s27, s21
	s_add_i32 s3, s3, -1
	s_and_b32 s31, s30, 0xc000
	s_add_i32 s33, s31, 0
	s_ashr_i32 s3, s3, 2
	s_add_i32 s31, s2, 0x7e0
	s_cmp_gt_i32 s31, s23
	v_cvt_f32_i32_e32 v111, s3
	s_cselect_b64 s[34:35], -1, 0
	s_add_i32 s3, s2, 0x7ff
	s_cmp_lt_i32 s3, s24
	s_cselect_b64 s[38:39], -1, 0
	v_add_u32_e32 v2, s33, v101
	v_add_u32_e32 v4, s33, v102
	v_add_u32_e32 v5, s33, v103
	v_add_u32_e32 v6, s33, v104
	s_or_b64 s[34:35], s[34:35], s[38:39]
	s_and_b64 vcc, exec, s[34:35]
	v_add_u32_e32 v115, v2, v100
	v_add_u32_e32 v114, v4, v100
	v_add_u32_e32 v113, v5, v100
	v_add_u32_e32 v112, v6, v100
	v_add_u32_e32 v16, s33, v105
	v_add_u32_e32 v17, s33, v106
	s_barrier
	s_cbranch_vccnz .LBB0_527
	ds_read_b128 v[4:7], v115 offset:4096
	ds_read_b128 v[188:191], v114 offset:4096
	ds_read_b128 v[192:195], v113 offset:4096
	ds_read_b128 v[202:205], v112 offset:4096
	s_and_b32 s31, s31, 0xe0
	v_or_b32_e32 v2, s31, v99
	v_cvt_f32_ubyte0_e32 v2, v2
	v_or_b32_sdwa v246, v2, v111 dst_sel:DWORD dst_unused:UNUSED_PAD src0_sel:DWORD src1_sel:WORD_1
	s_cmp_ge_i32 s20, s3
	s_cselect_b64 s[34:35], -1, 0
	s_waitcnt lgkmcnt(3)
	s_setprio 1
	v_mfma_f32_32x32x16_bf16 v[50:65], v[4:7], v[74:77], 0
	s_sub_i32 s3, s19, 32
	s_cmpk_lt_i32 s3, 0x1e1
	v_add3_u32 v116, v17, v94, s69
	s_cselect_b64 s[38:39], -1, 0
	s_and_b64 s[34:35], s[34:35], s[38:39]
	s_and_b64 vcc, exec, s[34:35]
	s_waitcnt lgkmcnt(2)
	v_mfma_f32_32x32x16_bf16 v[50:65], v[188:191], v[66:69], v[50:65]
	s_waitcnt lgkmcnt(1)
	v_mfma_f32_32x32x16_bf16 v[50:65], v[192:195], v[70:73], v[50:65]
	s_waitcnt lgkmcnt(0)
	v_mfma_f32_32x32x16_bf16 v[50:65], v[202:205], v[78:81], v[50:65]
	v_mfma_f32_32x32x16_bf16 v[50:65], v[246:249], v[82:85], v[50:65]
	v_add3_u32 v2, v16, v94, s69
	ds_read_b64_tr_b16 v[86:87], v2
	ds_read_b64_tr_b16 v[88:89], v2 offset:1024
	ds_read_b64_tr_b16 v[12:13], v116
	ds_read_b64_tr_b16 v[14:15], v116 offset:1024
	ds_read_b64_tr_b16 v[8:9], v2 offset:2048
	ds_read_b64_tr_b16 v[10:11], v2 offset:3072
	ds_read_b64_tr_b16 v[4:5], v116 offset:2048
	ds_read_b64_tr_b16 v[6:7], v116 offset:3072
	s_cbranch_vccnz .LBB0_524
	v_add_u32_e32 v2, s19, v108
	v_subrev_u32_e32 v116, 32, v2
	v_cmp_gt_u32_e32 vcc, s79, v116
	v_add3_u32 v116, v109, s22, 32
	s_nop 5
	v_cndmask_b32_e32 v50, v197, v50, vcc
	v_cmp_lt_u32_e32 vcc, s80, v116
	v_subrev_u32_e32 v116, 34, v2
	s_nop 0
	v_cndmask_b32_e32 v51, v197, v51, vcc
	v_cmp_gt_u32_e32 vcc, s79, v116
	v_subrev_u32_e32 v116, 35, v2
	s_nop 0
	v_cndmask_b32_e32 v52, v197, v52, vcc
	v_cmp_gt_u32_e32 vcc, s79, v116
	v_subrev_u32_e32 v116, 40, v2
	s_nop 0
	v_cndmask_b32_e32 v53, v197, v53, vcc
	v_cmp_gt_u32_e32 vcc, s79, v116
	v_subrev_u32_e32 v116, 41, v2
	s_nop 0
	v_cndmask_b32_e32 v54, v197, v54, vcc
	v_cmp_gt_u32_e32 vcc, s79, v116
	v_subrev_u32_e32 v116, 42, v2
	s_nop 0
	v_cndmask_b32_e32 v55, v197, v55, vcc
	v_cmp_gt_u32_e32 vcc, s79, v116
	v_subrev_u32_e32 v116, 43, v2
	s_nop 0
	v_cndmask_b32_e32 v56, v197, v56, vcc
	v_cmp_gt_u32_e32 vcc, s79, v116
	v_subrev_u32_e32 v116, 48, v2
	s_nop 0
	v_cndmask_b32_e32 v57, v197, v57, vcc
	v_cmp_gt_u32_e32 vcc, s79, v116
	v_subrev_u32_e32 v116, 49, v2
	s_nop 0
	v_cndmask_b32_e32 v58, v197, v58, vcc
	v_cmp_gt_u32_e32 vcc, s79, v116
	v_subrev_u32_e32 v116, 50, v2
	s_nop 0
	v_cndmask_b32_e32 v59, v197, v59, vcc
	v_cmp_gt_u32_e32 vcc, s79, v116
	v_subrev_u32_e32 v116, 51, v2
	s_nop 0
	v_cndmask_b32_e32 v60, v197, v60, vcc
	v_cmp_gt_u32_e32 vcc, s79, v116
	v_subrev_u32_e32 v116, 56, v2
	s_nop 0
	v_cndmask_b32_e32 v61, v197, v61, vcc
	v_cmp_gt_u32_e32 vcc, s79, v116
	v_subrev_u32_e32 v116, 57, v2
	s_nop 0
	v_cndmask_b32_e32 v62, v197, v62, vcc
	v_cmp_gt_u32_e32 vcc, s79, v116
	v_subrev_u32_e32 v116, 58, v2
	v_subrev_u32_e32 v2, 59, v2
	v_cndmask_b32_e32 v63, v197, v63, vcc
	v_cmp_gt_u32_e32 vcc, s79, v116
	s_nop 1
	v_cndmask_b32_e32 v64, v197, v64, vcc
	v_cmp_gt_u32_e32 vcc, s79, v2
	s_nop 1
	v_cndmask_b32_e32 v65, v197, v65, vcc

.Lring_issue_skip_0:
	s_add_i32 s3, s2, 0x7c0
	s_cmp_gt_i32 s3, s23
	s_cselect_b64 s[34:35], -1, 0
	s_addk_i32 s2, 0x7df
	s_cmp_lt_i32 s2, s24
	s_cselect_b64 s[38:39], -1, 0
	s_or_b64 s[34:35], s[34:35], s[38:39]
	s_and_b64 vcc, exec, s[34:35]
	s_cbranch_vccnz .LBB0_510
	ds_read_b128 v[4:7], v115
	ds_read_b128 v[188:191], v114
	ds_read_b128 v[192:195], v113
	ds_read_b128 v[202:205], v112
	s_and_b32 s3, s3, 0xc0
	v_or_b32_e32 v2, s3, v99
	v_cvt_f32_ubyte0_e32 v2, v2
	v_or_b32_sdwa v246, v2, v111 dst_sel:DWORD dst_unused:UNUSED_PAD src0_sel:DWORD src1_sel:WORD_1
	s_cmp_ge_i32 s20, s2
	s_cselect_b64 s[2:3], -1, 0
	s_waitcnt lgkmcnt(3)
	s_setprio 1
	v_mfma_f32_32x32x16_bf16 v[50:65], v[4:7], v[74:77], 0
	s_cmpk_lt_i32 s19, 0x1e1
	s_cselect_b64 s[34:35], -1, 0
	s_and_b64 s[2:3], s[2:3], s[34:35]
	s_and_b64 vcc, exec, s[2:3]
	s_waitcnt lgkmcnt(2)
	v_mfma_f32_32x32x16_bf16 v[50:65], v[188:191], v[66:69], v[50:65]
	s_waitcnt lgkmcnt(1)
	v_mfma_f32_32x32x16_bf16 v[50:65], v[192:195], v[70:73], v[50:65]
	s_waitcnt lgkmcnt(0)
	v_mfma_f32_32x32x16_bf16 v[50:65], v[202:205], v[78:81], v[50:65]
	v_mfma_f32_32x32x16_bf16 v[50:65], v[246:249], v[82:85], v[50:65]
	v_add3_u32 v2, v16, v94, s67
	v_add3_u32 v16, v17, v94, s67
	ds_read_b64_tr_b16 v[86:87], v2
	ds_read_b64_tr_b16 v[88:89], v2 offset:1024
	ds_read_b64_tr_b16 v[12:13], v16
	ds_read_b64_tr_b16 v[14:15], v16 offset:1024
	ds_read_b64_tr_b16 v[8:9], v2 offset:2048
	ds_read_b64_tr_b16 v[10:11], v2 offset:3072
	ds_read_b64_tr_b16 v[4:5], v16 offset:2048
	ds_read_b64_tr_b16 v[6:7], v16 offset:3072
	s_cbranch_vccnz .LBB0_530
	v_add_u32_e32 v2, s19, v108
	v_cmp_gt_u32_e32 vcc, s79, v2
	v_add_u32_e32 v16, s22, v109
	s_nop 5
	v_cndmask_b32_e32 v50, v197, v50, vcc
	v_cmp_lt_u32_e32 vcc, s80, v16
	v_add_u32_e32 v16, -2, v2
	s_nop 0
	v_cndmask_b32_e32 v51, v197, v51, vcc
	v_cmp_gt_u32_e32 vcc, s79, v16
	v_add_u32_e32 v16, -3, v2
	s_nop 0
	v_cndmask_b32_e32 v52, v197, v52, vcc
	v_cmp_gt_u32_e32 vcc, s79, v16
	v_add_u32_e32 v16, -8, v2
	s_nop 0
	v_cndmask_b32_e32 v53, v197, v53, vcc
	v_cmp_gt_u32_e32 vcc, s79, v16
	v_add_u32_e32 v16, -9, v2
	s_nop 0
	v_cndmask_b32_e32 v54, v197, v54, vcc
	v_cmp_gt_u32_e32 vcc, s79, v16
	v_add_u32_e32 v16, -10, v2
	s_nop 0
	v_cndmask_b32_e32 v55, v197, v55, vcc
	v_cmp_gt_u32_e32 vcc, s79, v16
	v_add_u32_e32 v16, -11, v2
	s_nop 0
	v_cndmask_b32_e32 v56, v197, v56, vcc
	v_cmp_gt_u32_e32 vcc, s79, v16
	v_add_u32_e32 v16, -16, v2
	s_nop 0
	v_cndmask_b32_e32 v57, v197, v57, vcc
	v_cmp_gt_u32_e32 vcc, s79, v16
	v_subrev_u32_e32 v16, 17, v2
	s_nop 0
	v_cndmask_b32_e32 v58, v197, v58, vcc
	v_cmp_gt_u32_e32 vcc, s79, v16
	v_subrev_u32_e32 v16, 18, v2
	s_nop 0
	v_cndmask_b32_e32 v59, v197, v59, vcc
	v_cmp_gt_u32_e32 vcc, s79, v16
	v_subrev_u32_e32 v16, 19, v2
	s_nop 0
	v_cndmask_b32_e32 v60, v197, v60, vcc
	v_cmp_gt_u32_e32 vcc, s79, v16
	v_subrev_u32_e32 v16, 24, v2
	s_nop 0
	v_cndmask_b32_e32 v61, v197, v61, vcc
	v_cmp_gt_u32_e32 vcc, s79, v16
	v_subrev_u32_e32 v16, 25, v2
	s_nop 0
	v_cndmask_b32_e32 v62, v197, v62, vcc
	v_cmp_gt_u32_e32 vcc, s79, v16
	v_subrev_u32_e32 v16, 26, v2
	v_subrev_u32_e32 v2, 27, v2
	v_cndmask_b32_e32 v63, v197, v63, vcc
	v_cmp_gt_u32_e32 vcc, s79, v16
	s_nop 1
	v_cndmask_b32_e32 v64, v197, v64, vcc
	v_cmp_gt_u32_e32 vcc, s79, v2
	s_nop 1
	v_cndmask_b32_e32 v65, v197, v65, vcc

.LBB0_681:
	s_flbit_i32_b32 s0, s2
	s_xor_b32 s0, s0, 31
	s_lshl_b32 s8, 1, s0
	s_waitcnt lgkmcnt(0)
	v_and_b32_e32 v2, s8, v136
	v_cmp_ne_u32_e64 s[38:39], 0, v2
	s_mov_b64 vcc, s[38:39]
	s_cbranch_vccz .LBB0_669
	s_and_b32 s1, s5, 0xc000
	s_lshl_b32 s9, s0, 6
	s_lshr_b32 s0, s0, 2
	s_xor_b32 s1, s1, 0x8000
	v_cvt_f32_u32_e32 v159, s0
	s_add_i32 s1, s1, 0
	v_add_u32_e32 v2, s1, v137
	v_add_u32_e32 v4, s1, v138
	v_add_u32_e32 v5, s1, v139
	v_add_u32_e32 v6, s1, v140
	s_or_b32 s10, s9, 32
	s_cmp_gt_i32 s10, s6
	v_add_u32_e32 v163, v2, v134
	v_add_u32_e32 v162, v4, v134
	v_add_u32_e32 v161, v5, v134
	v_add_u32_e32 v160, v6, v134
	v_add_u32_e32 v17, s1, v156
	v_add_u32_e32 v16, s1, v157
	s_cbranch_scc1 .LBB0_690
	ds_read_b128 v[4:7], v163 offset:4096
	ds_read_b128 v[188:191], v162 offset:4096
	ds_read_b128 v[192:195], v161 offset:4096
	ds_read_b128 v[202:205], v160 offset:4096
	s_and_b32 s0, s10, 0xe0
	v_or_b32_e32 v2, s0, v129
	v_cvt_f32_ubyte0_e32 v2, v2
	v_or_b32_sdwa v210, v2, v159 dst_sel:DWORD dst_unused:UNUSED_PAD src0_sel:DWORD src1_sel:WORD_1
	s_or_b32 s0, s9, 63
	s_cmp_lt_u32 s16, s0
	s_waitcnt lgkmcnt(3)
	s_setprio 1
	v_mfma_f32_32x32x16_bf16 v[82:97], v[4:7], v[106:109], 0
	s_cselect_b64 s[0:1], -1, 0
	s_sub_i32 s11, s16, s10
	s_cmp_gt_i32 s11, 0x3fffffe0
	v_add3_u32 v164, v16, v135, s69
	s_cselect_b64 s[12:13], -1, 0
	s_or_b64 s[0:1], s[0:1], s[12:13]
	s_and_b64 vcc, exec, s[0:1]
	s_waitcnt lgkmcnt(2)
	v_mfma_f32_32x32x16_bf16 v[82:97], v[188:191], v[98:101], v[82:97]
	s_waitcnt lgkmcnt(1)
	v_mfma_f32_32x32x16_bf16 v[82:97], v[192:195], v[102:105], v[82:97]
	s_waitcnt lgkmcnt(0)
	v_mfma_f32_32x32x16_bf16 v[82:97], v[202:205], v[110:113], v[82:97]
	v_mfma_f32_32x32x16_bf16 v[82:97], v[210:213], v[114:117], v[82:97]
	v_add3_u32 v2, v17, v135, s69
	ds_read_b64_tr_b16 v[118:119], v2
	ds_read_b64_tr_b16 v[120:121], v2 offset:1024
	ds_read_b64_tr_b16 v[12:13], v164
	ds_read_b64_tr_b16 v[14:15], v164 offset:1024
	ds_read_b64_tr_b16 v[8:9], v2 offset:2048
	ds_read_b64_tr_b16 v[10:11], v2 offset:3072
	ds_read_b64_tr_b16 v[4:5], v164 offset:2048
	ds_read_b64_tr_b16 v[6:7], v164 offset:3072
	s_cbranch_vccnz .LBB0_685
	v_cndmask_b32_e64 v2, 0, 1, s[38:39]
	v_cmp_ne_u32_e32 vcc, 0, v2
	s_cmp_lg_u64 vcc, exec
	s_cselect_b64 s[0:1], -1, 0
	s_cbranch_scc0 .LBB0_687
	v_cndmask_b32_e64 v82, v197, v82, s[38:39]
	v_cndmask_b32_e64 v83, v197, v83, s[38:39]
	v_cndmask_b32_e64 v84, v197, v84, s[38:39]
	v_cndmask_b32_e64 v85, v197, v85, s[38:39]
	v_cndmask_b32_e64 v86, v197, v86, s[38:39]
	v_cndmask_b32_e64 v87, v197, v87, s[38:39]
	v_cndmask_b32_e64 v88, v197, v88, s[38:39]
	v_cndmask_b32_e64 v89, v197, v89, s[38:39]
	v_cndmask_b32_e64 v90, v197, v90, s[38:39]
	v_cndmask_b32_e64 v91, v197, v91, s[38:39]
	v_cndmask_b32_e64 v92, v197, v92, s[38:39]
	v_cndmask_b32_e64 v93, v197, v93, s[38:39]
	v_cndmask_b32_e64 v94, v197, v94, s[38:39]
	v_cndmask_b32_e64 v95, v197, v95, s[38:39]
	v_cndmask_b32_e64 v96, v197, v96, s[38:39]
	v_cndmask_b32_e64 v97, v197, v97, s[38:39]
	s_branch .LBB0_687

.LBB0_690:
	s_cmp_gt_i32 s9, s6
	s_cbranch_scc1 .LBB0_669
	ds_read_b128 v[4:7], v163
	ds_read_b128 v[188:191], v162
	ds_read_b128 v[192:195], v161
	ds_read_b128 v[202:205], v160
	s_and_b32 s0, s9, 0xc0
	v_or_b32_e32 v2, s0, v129
	v_cvt_f32_ubyte0_e32 v2, v2
	v_or_b32_sdwa v210, v2, v159 dst_sel:DWORD dst_unused:UNUSED_PAD src0_sel:DWORD src1_sel:WORD_1
	s_or_b32 s0, s9, 31
	s_cmp_lt_i32 s16, s0
	s_waitcnt lgkmcnt(3)
	s_setprio 1
	v_mfma_f32_32x32x16_bf16 v[82:97], v[4:7], v[106:109], 0
	s_cselect_b64 s[0:1], -1, 0
	s_sub_i32 s10, s16, s9
	s_cmp_gt_i32 s10, 0x3fffffe0
	v_add3_u32 v16, v16, v135, s67
	s_cselect_b64 s[10:11], -1, 0
	s_or_b64 s[0:1], s[0:1], s[10:11]
	s_and_b64 vcc, exec, s[0:1]
	s_waitcnt lgkmcnt(2)
	v_mfma_f32_32x32x16_bf16 v[82:97], v[188:191], v[98:101], v[82:97]
	s_waitcnt lgkmcnt(1)
	v_mfma_f32_32x32x16_bf16 v[82:97], v[192:195], v[102:105], v[82:97]
	s_waitcnt lgkmcnt(0)
	v_mfma_f32_32x32x16_bf16 v[82:97], v[202:205], v[110:113], v[82:97]
	v_mfma_f32_32x32x16_bf16 v[82:97], v[210:213], v[114:117], v[82:97]
	v_add3_u32 v2, v17, v135, s67
	ds_read_b64_tr_b16 v[118:119], v2
	ds_read_b64_tr_b16 v[120:121], v2 offset:1024
	ds_read_b64_tr_b16 v[12:13], v16
	ds_read_b64_tr_b16 v[14:15], v16 offset:1024
	ds_read_b64_tr_b16 v[8:9], v2 offset:2048
	ds_read_b64_tr_b16 v[10:11], v2 offset:3072
	ds_read_b64_tr_b16 v[4:5], v16 offset:2048
	ds_read_b64_tr_b16 v[6:7], v16 offset:3072
	s_cbranch_vccnz .LBB0_693
	v_cndmask_b32_e64 v2, 0, 1, s[38:39]
	v_cmp_ne_u32_e32 vcc, 0, v2
	s_cmp_lg_u64 vcc, exec
	s_cselect_b64 s[0:1], -1, 0
	s_cbranch_scc0 .LBB0_695
	v_cndmask_b32_e64 v82, v197, v82, s[38:39]
	v_cndmask_b32_e64 v83, v197, v83, s[38:39]
	v_cndmask_b32_e64 v84, v197, v84, s[38:39]
	v_cndmask_b32_e64 v85, v197, v85, s[38:39]
	v_cndmask_b32_e64 v86, v197, v86, s[38:39]
	v_cndmask_b32_e64 v87, v197, v87, s[38:39]
	v_cndmask_b32_e64 v88, v197, v88, s[38:39]
	v_cndmask_b32_e64 v89, v197, v89, s[38:39]
	v_cndmask_b32_e64 v90, v197, v90, s[38:39]
	v_cndmask_b32_e64 v91, v197, v91, s[38:39]
	v_cndmask_b32_e64 v92, v197, v92, s[38:39]
	v_cndmask_b32_e64 v93, v197, v93, s[38:39]
	v_cndmask_b32_e64 v94, v197, v94, s[38:39]
	v_cndmask_b32_e64 v95, v197, v95, s[38:39]
	v_cndmask_b32_e64 v96, v197, v96, s[38:39]
	v_cndmask_b32_e64 v97, v197, v97, s[38:39]
	s_branch .LBB0_695

.Lw_swa_4_done:
.LBB0_780:
	s_cmp_eq_u32 s32, 0
	s_cselect_b32 s84, 0, 1
	s_sub_u32 s32, s32, s84
	s_add_i32 s0, s25, s17
	s_add_i32 s1, s23, s18
	s_add_i32 s1, s1, -1
	s_and_b32 s27, s26, 0xc000
	s_add_i32 s34, s27, 0
	s_ashr_i32 s1, s1, 2
	s_add_i32 s27, s0, 0x7e0
	s_cmp_gt_i32 s27, s19
	v_cvt_f32_i32_e32 v114, s1
	s_cselect_b64 s[28:29], -1, 0
	s_add_i32 s1, s0, 0x7ff
	s_cmp_lt_i32 s1, s20
	s_cselect_b64 s[30:31], -1, 0
	v_add_u32_e32 v2, s34, v104
	v_add_u32_e32 v4, s34, v105
	v_add_u32_e32 v5, s34, v106
	v_add_u32_e32 v6, s34, v107
	s_or_b64 s[28:29], s[28:29], s[30:31]
	s_and_b64 vcc, exec, s[28:29]
	v_add_u32_e32 v118, v2, v103
	v_add_u32_e32 v117, v4, v103
	v_add_u32_e32 v116, v5, v103
	v_add_u32_e32 v115, v6, v103
	v_add_u32_e32 v16, s34, v109
	v_add_u32_e32 v17, s34, v110
	s_barrier
	s_cbranch_vccnz .LBB0_788
	ds_read_b128 v[4:7], v118 offset:4096
	ds_read_b128 v[188:191], v117 offset:4096
	ds_read_b128 v[192:195], v116 offset:4096
	ds_read_b128 v[202:205], v115 offset:4096
	s_and_b32 s27, s27, 0xe0
	v_or_b32_e32 v2, s27, v102
	v_cvt_f32_ubyte0_e32 v2, v2
	v_or_b32_sdwa v246, v2, v114 dst_sel:DWORD dst_unused:UNUSED_PAD src0_sel:DWORD src1_sel:WORD_1
	s_cmp_ge_i32 s16, s1
	s_cselect_b64 s[28:29], -1, 0
	s_waitcnt lgkmcnt(3)
	s_setprio 1
	v_mfma_f32_32x32x16_bf16 v[50:65], v[4:7], v[66:69], 0
	s_sub_i32 s1, s15, 32
	s_cmpk_lt_i32 s1, 0x61
	v_add3_u32 v119, v17, v96, s69
	s_cselect_b64 s[30:31], -1, 0
	s_and_b64 s[28:29], s[28:29], s[30:31]
	s_and_b64 vcc, exec, s[28:29]
	s_waitcnt lgkmcnt(2)
	v_mfma_f32_32x32x16_bf16 v[50:65], v[188:191], v[70:73], v[50:65]
	s_waitcnt lgkmcnt(1)
	v_mfma_f32_32x32x16_bf16 v[50:65], v[192:195], v[74:77], v[50:65]
	s_waitcnt lgkmcnt(0)
	v_mfma_f32_32x32x16_bf16 v[50:65], v[202:205], v[78:81], v[50:65]
	v_mfma_f32_32x32x16_bf16 v[50:65], v[246:249], v[82:85], v[50:65]
	v_add3_u32 v2, v16, v96, s69
	ds_read_b64_tr_b16 v[86:87], v2
	ds_read_b64_tr_b16 v[88:89], v2 offset:1024
	ds_read_b64_tr_b16 v[12:13], v119
	ds_read_b64_tr_b16 v[14:15], v119 offset:1024
	ds_read_b64_tr_b16 v[8:9], v2 offset:2048
	ds_read_b64_tr_b16 v[10:11], v2 offset:3072
	ds_read_b64_tr_b16 v[4:5], v119 offset:2048
	ds_read_b64_tr_b16 v[6:7], v119 offset:3072
	s_cbranch_vccnz .LBB0_785
	v_add_u32_e32 v2, s15, v111
	v_subrev_u32_e32 v119, 32, v2
	v_cmp_gt_u32_e32 vcc, s71, v119
	v_add3_u32 v119, v112, s17, 32
	s_nop 5
	v_cndmask_b32_e32 v50, v197, v50, vcc
	v_cmp_lt_u32_e32 vcc, s47, v119
	v_subrev_u32_e32 v119, 34, v2
	s_nop 0
	v_cndmask_b32_e32 v51, v197, v51, vcc
	v_cmp_gt_u32_e32 vcc, s71, v119
	v_subrev_u32_e32 v119, 35, v2
	s_nop 0
	v_cndmask_b32_e32 v52, v197, v52, vcc
	v_cmp_gt_u32_e32 vcc, s71, v119
	v_subrev_u32_e32 v119, 40, v2
	s_nop 0
	v_cndmask_b32_e32 v53, v197, v53, vcc
	v_cmp_gt_u32_e32 vcc, s71, v119
	v_subrev_u32_e32 v119, 41, v2
	s_nop 0
	v_cndmask_b32_e32 v54, v197, v54, vcc
	v_cmp_gt_u32_e32 vcc, s71, v119
	v_subrev_u32_e32 v119, 42, v2
	s_nop 0
	v_cndmask_b32_e32 v55, v197, v55, vcc
	v_cmp_gt_u32_e32 vcc, s71, v119
	v_subrev_u32_e32 v119, 43, v2
	s_nop 0
	v_cndmask_b32_e32 v56, v197, v56, vcc
	v_cmp_gt_u32_e32 vcc, s71, v119
	v_subrev_u32_e32 v119, 48, v2
	s_nop 0
	v_cndmask_b32_e32 v57, v197, v57, vcc
	v_cmp_gt_u32_e32 vcc, s71, v119
	v_subrev_u32_e32 v119, 49, v2
	s_nop 0
	v_cndmask_b32_e32 v58, v197, v58, vcc
	v_cmp_gt_u32_e32 vcc, s71, v119
	v_subrev_u32_e32 v119, 50, v2
	s_nop 0
	v_cndmask_b32_e32 v59, v197, v59, vcc
	v_cmp_gt_u32_e32 vcc, s71, v119
	v_subrev_u32_e32 v119, 51, v2
	s_nop 0
	v_cndmask_b32_e32 v60, v197, v60, vcc
	v_cmp_gt_u32_e32 vcc, s71, v119
	v_subrev_u32_e32 v119, 56, v2
	s_nop 0
	v_cndmask_b32_e32 v61, v197, v61, vcc
	v_cmp_gt_u32_e32 vcc, s71, v119
	v_subrev_u32_e32 v119, 57, v2
	s_nop 0
	v_cndmask_b32_e32 v62, v197, v62, vcc
	v_cmp_gt_u32_e32 vcc, s71, v119
	v_subrev_u32_e32 v119, 58, v2
	v_subrev_u32_e32 v2, 59, v2
	v_cndmask_b32_e32 v63, v197, v63, vcc
	v_cmp_gt_u32_e32 vcc, s71, v119
	s_nop 1
	v_cndmask_b32_e32 v64, v197, v64, vcc
	v_cmp_gt_u32_e32 vcc, s71, v2
	s_nop 1
	v_cndmask_b32_e32 v65, v197, v65, vcc

.Lring_issue_skip_1:
	s_add_i32 s1, s0, 0x7c0
	s_cmp_gt_i32 s1, s19
	s_cselect_b64 s[28:29], -1, 0
	s_addk_i32 s0, 0x7df
	s_cmp_lt_i32 s0, s20
	s_cselect_b64 s[30:31], -1, 0
	s_or_b64 s[28:29], s[28:29], s[30:31]
	s_and_b64 vcc, exec, s[28:29]
	s_cbranch_vccnz .LBB0_771
	ds_read_b128 v[4:7], v118
	ds_read_b128 v[188:191], v117
	ds_read_b128 v[192:195], v116
	ds_read_b128 v[202:205], v115
	s_and_b32 s1, s1, 0xc0
	v_or_b32_e32 v2, s1, v102
	v_cvt_f32_ubyte0_e32 v2, v2
	v_or_b32_sdwa v246, v2, v114 dst_sel:DWORD dst_unused:UNUSED_PAD src0_sel:DWORD src1_sel:WORD_1
	s_cmp_ge_i32 s16, s0
	s_cselect_b64 s[0:1], -1, 0
	s_waitcnt lgkmcnt(3)
	s_setprio 1
	v_mfma_f32_32x32x16_bf16 v[50:65], v[4:7], v[66:69], 0
	s_cmpk_lt_i32 s15, 0x61
	s_cselect_b64 s[28:29], -1, 0
	s_and_b64 s[0:1], s[0:1], s[28:29]
	s_and_b64 vcc, exec, s[0:1]
	s_waitcnt lgkmcnt(2)
	v_mfma_f32_32x32x16_bf16 v[50:65], v[188:191], v[70:73], v[50:65]
	s_waitcnt lgkmcnt(1)
	v_mfma_f32_32x32x16_bf16 v[50:65], v[192:195], v[74:77], v[50:65]
	s_waitcnt lgkmcnt(0)
	v_mfma_f32_32x32x16_bf16 v[50:65], v[202:205], v[78:81], v[50:65]
	v_mfma_f32_32x32x16_bf16 v[50:65], v[246:249], v[82:85], v[50:65]
	v_add3_u32 v2, v16, v96, s67
	v_add3_u32 v16, v17, v96, s67
	ds_read_b64_tr_b16 v[86:87], v2
	ds_read_b64_tr_b16 v[88:89], v2 offset:1024
	ds_read_b64_tr_b16 v[12:13], v16
	ds_read_b64_tr_b16 v[14:15], v16 offset:1024
	ds_read_b64_tr_b16 v[8:9], v2 offset:2048
	ds_read_b64_tr_b16 v[10:11], v2 offset:3072
	ds_read_b64_tr_b16 v[4:5], v16 offset:2048
	ds_read_b64_tr_b16 v[6:7], v16 offset:3072
	s_cbranch_vccnz .LBB0_791
	v_add_u32_e32 v2, s15, v111
	v_cmp_gt_u32_e32 vcc, s71, v2
	v_add_u32_e32 v16, s17, v112
	s_nop 5
	v_cndmask_b32_e32 v50, v197, v50, vcc
	v_cmp_lt_u32_e32 vcc, s47, v16
	v_add_u32_e32 v16, -2, v2
	s_nop 0
	v_cndmask_b32_e32 v51, v197, v51, vcc
	v_cmp_gt_u32_e32 vcc, s71, v16
	v_add_u32_e32 v16, -3, v2
	s_nop 0
	v_cndmask_b32_e32 v52, v197, v52, vcc
	v_cmp_gt_u32_e32 vcc, s71, v16
	v_add_u32_e32 v16, -8, v2
	s_nop 0
	v_cndmask_b32_e32 v53, v197, v53, vcc
	v_cmp_gt_u32_e32 vcc, s71, v16
	v_add_u32_e32 v16, -9, v2
	s_nop 0
	v_cndmask_b32_e32 v54, v197, v54, vcc
	v_cmp_gt_u32_e32 vcc, s71, v16
	v_add_u32_e32 v16, -10, v2
	s_nop 0
	v_cndmask_b32_e32 v55, v197, v55, vcc
	v_cmp_gt_u32_e32 vcc, s71, v16
	v_add_u32_e32 v16, -11, v2
	s_nop 0
	v_cndmask_b32_e32 v56, v197, v56, vcc
	v_cmp_gt_u32_e32 vcc, s71, v16
	v_add_u32_e32 v16, -16, v2
	s_nop 0
	v_cndmask_b32_e32 v57, v197, v57, vcc
	v_cmp_gt_u32_e32 vcc, s71, v16
	v_subrev_u32_e32 v16, 17, v2
	s_nop 0
	v_cndmask_b32_e32 v58, v197, v58, vcc
	v_cmp_gt_u32_e32 vcc, s71, v16
	v_subrev_u32_e32 v16, 18, v2
	s_nop 0
	v_cndmask_b32_e32 v59, v197, v59, vcc
	v_cmp_gt_u32_e32 vcc, s71, v16
	v_subrev_u32_e32 v16, 19, v2
	s_nop 0
	v_cndmask_b32_e32 v60, v197, v60, vcc
	v_cmp_gt_u32_e32 vcc, s71, v16
	v_subrev_u32_e32 v16, 24, v2
	s_nop 0
	v_cndmask_b32_e32 v61, v197, v61, vcc
	v_cmp_gt_u32_e32 vcc, s71, v16
	v_subrev_u32_e32 v16, 25, v2
	s_nop 0
	v_cndmask_b32_e32 v62, v197, v62, vcc
	v_cmp_gt_u32_e32 vcc, s71, v16
	v_subrev_u32_e32 v16, 26, v2
	v_subrev_u32_e32 v2, 27, v2
	v_cndmask_b32_e32 v63, v197, v63, vcc
	v_cmp_gt_u32_e32 vcc, s71, v16
	s_nop 1
	v_cndmask_b32_e32 v64, v197, v64, vcc
	v_cmp_gt_u32_e32 vcc, s71, v2
	s_nop 1
	v_cndmask_b32_e32 v65, v197, v65, vcc
